# baseline (speedup 1.0000x reference)
_ZN12_GLOBAL__N_113search_kernelEPKfS1_PhPf:
	s_load_dwordx2 s[8:9], s[0:1], 0x0
	s_load_dwordx2 s[4:5], s[0:1], 0x10
	s_movk_i32 s3, 0x90
	v_readfirstlane_b32 s10, v0
	v_cmp_gt_u32_e32 vcc, s3, v0
	s_and_saveexec_b64 s[6:7], vcc
	v_mov_b32_e32 v2, -1
	v_lshlrev_b32_e32 v1, 3, v0
	v_mov_b32_e32 v3, v2
	ds_write_b64 v1, v[2:3] offset:16384
	s_or_b64 exec, exec, s[6:7]
	s_waitcnt lgkmcnt(0)
	s_lshl_b32 s20, s2, 1
	s_and_b32 s20, s20, 14
	s_ashr_i32 s21, s2, 7
	s_add_i32 s38, s20, s21
	s_bfe_u32 s39, s2, 0x40003
	s_lshr_b32 s21, s10, 6
	s_mul_i32 s21, s21, 24
	s_min_u32 s21, s21, 0xa5
	s_mul_i32 s20, s38, 0x90
	s_mul_i32 s60, s39, 9
	s_add_i32 s20, s20, s60
	s_lshl_b32 s20, s20, 10
	s_mul_i32 s60, s38, 0xbd
	s_add_i32 s21, s60, s21
	s_lshl_b32 s21, s21, 10
	v_and_b32_e32 v1, 63, v0
	v_lshl_add_u32 v164, v1, 4, s20
	v_lshl_add_u32 v165, v1, 4, s21
	s_add_u32 s22, s4, 0x1000
	s_addc_u32 s23, s5, 0
	s_add_u32 s24, s4, 0x2000
	s_addc_u32 s25, s5, 0
	s_add_u32 s26, s4, 0x240000
	s_addc_u32 s27, s5, 0
	s_add_u32 s28, s4, 0x241000
	s_addc_u32 s29, s5, 0
	s_add_u32 s30, s4, 0x242000
	s_addc_u32 s31, s5, 0
	s_add_u32 s32, s4, 0x243000
	s_addc_u32 s33, s5, 0
	s_add_u32 s34, s4, 0x244000
	s_addc_u32 s35, s5, 0
	s_add_u32 s36, s4, 0x245000
	s_addc_u32 s37, s5, 0
	global_load_dwordx4 v[112:115], v164, s[4:5]
	global_load_dwordx4 v[16:19], v165, s[26:27] nt
	global_load_dwordx4 v[20:23], v165, s[26:27] offset:1024 nt
	global_load_dwordx4 v[24:27], v165, s[26:27] offset:2048 nt
	global_load_dwordx4 v[28:31], v165, s[26:27] offset:3072 nt
	global_load_dwordx4 v[32:35], v165, s[28:29] nt
	global_load_dwordx4 v[36:39], v165, s[28:29] offset:1024 nt
	global_load_dwordx4 v[40:43], v165, s[28:29] offset:2048 nt
	global_load_dwordx4 v[44:47], v165, s[28:29] offset:3072 nt
	global_load_dwordx4 v[48:51], v165, s[30:31] nt
	global_load_dwordx4 v[52:55], v165, s[30:31] offset:1024 nt
	global_load_dwordx4 v[56:59], v165, s[30:31] offset:2048 nt
	global_load_dwordx4 v[60:63], v165, s[30:31] offset:3072 nt
	global_load_dwordx4 v[64:67], v165, s[32:33] nt
	global_load_dwordx4 v[68:71], v165, s[32:33] offset:1024 nt
	global_load_dwordx4 v[72:75], v165, s[32:33] offset:2048 nt
	global_load_dwordx4 v[76:79], v165, s[32:33] offset:3072 nt
	global_load_dwordx4 v[80:83], v165, s[34:35] nt
	global_load_dwordx4 v[84:87], v165, s[34:35] offset:1024 nt
	global_load_dwordx4 v[88:91], v165, s[34:35] offset:2048 nt
	global_load_dwordx4 v[92:95], v165, s[34:35] offset:3072 nt
	global_load_dwordx4 v[96:99], v165, s[36:37] nt
	global_load_dwordx4 v[100:103], v165, s[36:37] offset:1024 nt
	global_load_dwordx4 v[104:107], v165, s[36:37] offset:2048 nt
	global_load_dwordx4 v[108:111], v165, s[36:37] offset:3072 nt
	global_load_dwordx4 v[116:119], v164, s[4:5] offset:1024
	s_add_u32 s6, s4, 0x240000
	s_addc_u32 s7, s5, 0
	s_lshl_b32 s11, s2, 1
	s_and_b32 s14, s11, 14
	s_ashr_i32 s11, s2, 7
	s_lshr_b32 s15, s10, 6
	s_add_i32 s14, s14, s11
	s_bfe_u32 s2, s2, 0x40003
	s_mul_i32 s11, s15, 24
	v_mul_u32_u24_e32 v2, 0x71d, v0
	v_mul_u32_u24_e32 v4, 0x195, v0
	s_min_u32 s18, s11, 0xa5
	s_mul_i32 s11, s14, 3
	s_mul_i32 s12, s2, 9
	s_mov_b32 s13, 0
	v_lshrrev_b32_e32 v3, 16, v2
	s_movk_i32 s19, 0xffdc
	v_lshrrev_b32_e32 v5, 17, v4
	v_mad_i32_i24 v2, v3, s19, v0
	v_mad_i32_i24 v4, v5, -9, v3
	v_add_u32_e32 v3, s11, v5
	v_mov_b64_e32 v[6:7], s[12:13]
	v_mad_i64_i32 v[8:9], s[16:17], v3, s3, v[6:7]
	v_ashrrev_i32_e32 v5, 31, v4
	v_lshl_add_u64 v[4:5], v[8:9], 0, v[4:5]
	s_movk_i32 s13, 0x240
	v_mov_b64_e32 v[8:9], s[8:9]
	v_mad_u64_u32 v[10:11], s[8:9], v4, s13, v[8:9]
	v_min_u32_e32 v4, 0x1cb, v0
	v_or_b32_e32 v4, 0x200, v4
	v_mad_i32_i24 v11, v5, s13, v11
	v_mul_u32_u24_e32 v5, 0x71d, v4
	v_ashrrev_i32_e32 v3, 31, v2
	v_lshrrev_b32_e32 v5, 16, v5
	v_lshl_add_u64 v[2:3], v[2:3], 4, v[10:11]
	v_mad_i32_i24 v10, v5, s19, v4
	v_mul_u32_u24_e32 v4, 0x653, v4
	v_lshrrev_b32_e32 v11, 19, v4
	v_mad_i32_i24 v4, v11, -9, v5
	v_add_u32_e32 v5, s11, v11
	v_mad_i64_i32 v[6:7], s[8:9], v5, s3, v[6:7]
	v_ashrrev_i32_e32 v5, 31, v4
	v_lshl_add_u64 v[4:5], v[6:7], 0, v[4:5]
	v_mad_u64_u32 v[12:13], s[8:9], v4, s13, v[8:9]
	s_mul_i32 s8, s14, 0x90
	s_barrier
	s_load_dwordx2 s[42:43], s[0:1], 0x8
	s_load_dwordx2 s[62:63], s[0:1], 0x0
	v_mov_b32_e32 v244, v2
	v_mov_b32_e32 v245, v3
	global_load_dwordx4 v[6:9], v[2:3], off
	v_mad_i32_i24 v13, v5, s13, v13
	v_ashrrev_i32_e32 v11, 31, v10
	v_lshl_add_u64 v[10:11], v[10:11], 4, v[12:13]
	v_mov_b32_e32 v246, v10
	v_mov_b32_e32 v247, v11
	global_load_dwordx4 v[10:13], v[10:11], off
	s_mul_i32 s9, s14, 0xbd
	v_bfe_u32 v166, v0, 4, 2
	v_and_b32_e32 v167, 15, v0
	v_lshlrev_b32_e32 v167, 3, v167
	s_mul_i32 s40, s15, 6
	s_mov_b32 s41, 0x7f000000
	v_lshlrev_b32_e32 v14, 4, v0
	s_lshr_b32 s50, s15, 1
	s_and_b32 s51, s15, 1
	s_lshl_b32 s51, s51, 3
	s_mov_b32 s48, 0x1010101
	s_mov_b32 s49, 0x1010101
	s_movk_i32 s58, 0x900
	s_movk_i32 s59, 0xb40
	v_and_b32_e32 v168, 7, v0
	v_lshrrev_b32_e32 v177, 3, v1
	v_or_b32_e32 v177, s51, v177
	v_lshlrev_b32_e32 v169, 3, v177
	v_and_b32_e32 v179, 3, v0
	v_lshlrev_b32_e32 v179, 8, v179
	v_lshl_add_u32 v170, v177, 4, v179
	v_add_u32_e32 v170, s20, v170
	v_lshrrev_b32_e32 v179, 2, v168
	v_and_b32_e32 v180, 3, v0
	v_lshl_or_b32 v171, v179, 4, v180
	v_mul_u32_u24_e32 v179, 11, v168
	v_lshrrev_b32_e32 v179, 5, v179
	v_mul_u32_u24_e32 v180, 3, v179
	v_sub_u32_e32 v180, v168, v180
	v_mul_u32_u24_e32 v181, 0x90, v179
	v_add_u32_e32 v181, v181, v180
	v_mul_u32_u24_e32 v172, 0x240, v181
	v_mul_u32_u24_e32 v181, 0x48, v179
	v_add_u32_e32 v181, v181, v180
	v_mul_u32_u24_e32 v173, 0x120, v181
	v_mul_u32_u24_e32 v181, 0x24, v179
	v_add_u32_e32 v181, v181, v180
	v_mul_u32_u24_e32 v174, 0x90, v181
	v_mul_u32_u24_e32 v181, 9, v179
	v_add_u32_e32 v181, v181, v180
	v_mul_u32_u24_e32 v175, 0x240, v181
	v_add_u32_e32 v176, 8, v168
	s_waitcnt lgkmcnt(0)
	s_mul_i32 s60, s14, 0x3cc00
	s_add_u32 s42, s42, s60
	s_addc_u32 s43, s43, 0
	s_mul_i32 s60, s14, 0xf300
	s_add_u32 s44, s4, s60
	s_addc_u32 s45, s5, 0
	s_add_u32 s44, s44, 0x534000
	s_addc_u32 s45, s45, 0
	s_mul_i32 s60, s14, 0x3cc0
	s_add_u32 s46, s4, s60
	s_addc_u32 s47, s5, 0
	s_add_u32 s46, s46, 0x627000
	s_addc_u32 s47, s47, 0
	v_mov_b32_e32 v152, s42
	v_mov_b32_e32 v153, s43
	v_mov_b32_e32 v154, s44
	v_mov_b32_e32 v155, s45
	v_mov_b32_e32 v159, s46
	v_mov_b32_e32 v161, s47
	s_sub_u32 s60, s42, s62
	s_subb_u32 s61, s43, s63
	s_mul_i32 s62, s14, 0x3cc00
	s_sub_u32 s60, s60, s62
	s_subb_u32 s61, s61, 0
	v_lshl_add_u64 v[244:245], v[244:245], 0, s[60:61]
	v_lshl_add_u64 v[246:247], v[246:247], 0, s[60:61]
	s_lshl_b32 s62, s15, 10
	s_add_i32 s62, s62, 0x46e0
	s_mov_b32 m0, s62
	s_mul_i32 s62, s2, 0xf30
	s_add_u32 s60, s44, s62
	s_addc_u32 s61, s45, 0
	v_lshlrev_b32_e32 v240, 4, v0
	v_mov_b32_e32 v241, 0
	v_lshl_add_u64 v[240:241], v[240:241], 0, s[60:61]
	s_mul_i32 s62, s2, 0x3cc
	s_add_u32 s60, s46, s62
	s_addc_u32 s61, s47, 0
	v_lshlrev_b32_e32 v242, 2, v0
	v_mov_b32_e32 v243, 0
	v_lshl_add_u64 v[242:243], v[242:243], 0, s[60:61]
	global_load_lds_dwordx4 v[244:245], off
	global_load_lds_dwordx4 v[246:247], off
	global_load_lds_dwordx4 v[240:241], off
	global_load_lds_dword v[242:243], off
	s_load_dwordx2 s[2:3], s[0:1], 0x18
	s_waitcnt vmcnt(27)
	v_mfma_f32_16x16x32_f16 v[120:123], v[16:19], v[112:115], 0
	v_mfma_f32_16x16x32_f16 v[124:127], v[20:23], v[112:115], 0
	v_mfma_f32_16x16x32_f16 v[128:131], v[24:27], v[112:115], 0
	v_mfma_f32_16x16x32_f16 v[132:135], v[28:31], v[112:115], 0
	s_waitcnt vmcnt(23)
	v_mfma_f32_16x16x32_f16 v[136:139], v[32:35], v[112:115], 0
	v_mfma_f32_16x16x32_f16 v[140:143], v[36:39], v[112:115], 0
	v_mfma_f32_16x16x32_f16 v[144:147], v[40:43], v[112:115], 0
	v_mfma_f32_16x16x32_f16 v[148:151], v[44:47], v[112:115], 0
	v_min3_i32 v160, v120, v121, s41
	v_min3_i32 v160, v122, v123, v160
	v_min3_i32 v160, v124, v125, v160
	v_min3_i32 v160, v126, v127, v160
	v_min3_i32 v160, v128, v129, v160
	v_min3_i32 v160, v130, v131, v160
	v_min3_i32 v160, v132, v133, v160
	v_min3_i32 v157, v134, v135, v160
	s_waitcnt vmcnt(19)
	v_mfma_f32_16x16x32_f16 v[120:123], v[48:51], v[112:115], 0
	v_mfma_f32_16x16x32_f16 v[124:127], v[52:55], v[112:115], 0
	v_mov_b32_e32 v158, 0
	v_mfma_f32_16x16x32_f16 v[128:131], v[56:59], v[112:115], 0
	v_mfma_f32_16x16x32_f16 v[132:135], v[60:63], v[112:115], 0
	v_min3_i32 v160, v136, v137, v157
	v_min3_i32 v160, v138, v139, v160
	v_min3_i32 v160, v140, v141, v160
	v_min3_i32 v160, v142, v143, v160
	v_min3_i32 v160, v144, v145, v160
	v_min3_i32 v160, v146, v147, v160
	v_min3_i32 v160, v148, v149, v160
	v_min3_i32 v156, v150, v151, v160
	v_cmp_ge_i32_e32 vcc, v156, v157
	s_waitcnt vmcnt(15)
	v_mfma_f32_16x16x32_f16 v[136:139], v[64:67], v[112:115], 0
	v_mfma_f32_16x16x32_f16 v[140:143], v[68:71], v[112:115], 0
	v_cndmask_b32_e32 v158, 1, v158, vcc
	v_mfma_f32_16x16x32_f16 v[144:147], v[72:75], v[112:115], 0
	v_mfma_f32_16x16x32_f16 v[148:151], v[76:79], v[112:115], 0
	v_min3_i32 v160, v120, v121, v156
	v_min3_i32 v160, v122, v123, v160
	v_min3_i32 v160, v124, v125, v160
	v_min3_i32 v160, v126, v127, v160
	v_min3_i32 v160, v128, v129, v160
	v_min3_i32 v160, v130, v131, v160
	v_min3_i32 v160, v132, v133, v160
	v_min3_i32 v157, v134, v135, v160
	v_cmp_ge_i32_e32 vcc, v157, v156
	s_waitcnt vmcnt(11)
	v_mfma_f32_16x16x32_f16 v[120:123], v[80:83], v[112:115], 0
	v_mfma_f32_16x16x32_f16 v[124:127], v[84:87], v[112:115], 0
	v_cndmask_b32_e32 v158, 2, v158, vcc
	v_mfma_f32_16x16x32_f16 v[128:131], v[88:91], v[112:115], 0
	v_mfma_f32_16x16x32_f16 v[132:135], v[92:95], v[112:115], 0
	v_min3_i32 v160, v136, v137, v157
	v_min3_i32 v160, v138, v139, v160
	v_min3_i32 v160, v140, v141, v160
	v_min3_i32 v160, v142, v143, v160
	v_min3_i32 v160, v144, v145, v160
	v_min3_i32 v160, v146, v147, v160
	v_min3_i32 v160, v148, v149, v160
	v_min3_i32 v156, v150, v151, v160
	v_cmp_ge_i32_e32 vcc, v156, v157
	s_waitcnt vmcnt(7)
	v_mfma_f32_16x16x32_f16 v[136:139], v[96:99], v[112:115], 0
	v_mfma_f32_16x16x32_f16 v[140:143], v[100:103], v[112:115], 0
	v_cndmask_b32_e32 v158, 3, v158, vcc
	v_mfma_f32_16x16x32_f16 v[144:147], v[104:107], v[112:115], 0
	v_mfma_f32_16x16x32_f16 v[148:151], v[108:111], v[112:115], 0
	v_min3_i32 v160, v120, v121, v156
	v_min3_i32 v160, v122, v123, v160
	v_min3_i32 v160, v124, v125, v160
	v_min3_i32 v160, v126, v127, v160
	v_min3_i32 v160, v128, v129, v160
	v_min3_i32 v160, v130, v131, v160
	v_min3_i32 v160, v132, v133, v160
	v_min3_i32 v157, v134, v135, v160
	v_cmp_ge_i32_e32 vcc, v157, v156
	s_waitcnt vmcnt(4)
	ds_write_b128 v14, v[6:9]
	ds_write_b128 v14, v[10:13] offset:8192
	s_nop 0
	v_mov_b32_e32 v6, 0
	v_mov_b32_e32 v7, 0x900
	v_mov_b32_e32 v8, 0x240
	global_load_dwordx4 v[112:115], v164, s[4:5] offset:2048
	v_mfma_f32_16x16x32_f16 v[120:123], v[16:19], v[116:119], 0
	v_mfma_f32_16x16x32_f16 v[124:127], v[20:23], v[116:119], 0
	v_cndmask_b32_e32 v158, 4, v158, vcc
	v_mfma_f32_16x16x32_f16 v[128:131], v[24:27], v[116:119], 0
	v_mfma_f32_16x16x32_f16 v[132:135], v[28:31], v[116:119], 0
	v_min3_i32 v160, v136, v137, v157
	v_min3_i32 v160, v138, v139, v160
	v_min3_i32 v160, v140, v141, v160
	v_min3_i32 v160, v142, v143, v160
	v_min3_i32 v160, v144, v145, v160
	v_min3_i32 v160, v146, v147, v160
	v_min3_i32 v160, v148, v149, v160
	v_min3_i32 v156, v150, v151, v160
	v_cmp_ge_i32_e32 vcc, v156, v157
	v_mfma_f32_16x16x32_f16 v[136:139], v[32:35], v[116:119], 0
	v_mfma_f32_16x16x32_f16 v[140:143], v[36:39], v[116:119], 0
	v_cndmask_b32_e32 v158, 5, v158, vcc
	v_add_u32_e32 v162, s40, v158
	v_lshl_or_b32 v162, v162, 2, v166
	v_mov_b32_e32 v163, v156
	ds_min_u64 v167, v[162:163] offset:16384
	v_mfma_f32_16x16x32_f16 v[144:147], v[40:43], v[116:119], 0
	v_mfma_f32_16x16x32_f16 v[148:151], v[44:47], v[116:119], 0
	v_min3_i32 v160, v120, v121, s41
	v_min3_i32 v160, v122, v123, v160
	v_min3_i32 v160, v124, v125, v160
	v_min3_i32 v160, v126, v127, v160
	v_min3_i32 v160, v128, v129, v160
	v_min3_i32 v160, v130, v131, v160
	v_min3_i32 v160, v132, v133, v160
	v_min3_i32 v157, v134, v135, v160
	v_mfma_f32_16x16x32_f16 v[120:123], v[48:51], v[116:119], 0
	v_mfma_f32_16x16x32_f16 v[124:127], v[52:55], v[116:119], 0
	v_mov_b32_e32 v158, 0
	v_mfma_f32_16x16x32_f16 v[128:131], v[56:59], v[116:119], 0
	v_mfma_f32_16x16x32_f16 v[132:135], v[60:63], v[116:119], 0
	v_min3_i32 v160, v136, v137, v157
	v_min3_i32 v160, v138, v139, v160
	v_min3_i32 v160, v140, v141, v160
	v_min3_i32 v160, v142, v143, v160
	v_min3_i32 v160, v144, v145, v160
	v_min3_i32 v160, v146, v147, v160
	v_min3_i32 v160, v148, v149, v160
	v_min3_i32 v156, v150, v151, v160
	v_cmp_ge_i32_e32 vcc, v156, v157
	v_mfma_f32_16x16x32_f16 v[136:139], v[64:67], v[116:119], 0
	v_mfma_f32_16x16x32_f16 v[140:143], v[68:71], v[116:119], 0
	v_cndmask_b32_e32 v158, 1, v158, vcc
	v_mfma_f32_16x16x32_f16 v[144:147], v[72:75], v[116:119], 0
	v_mfma_f32_16x16x32_f16 v[148:151], v[76:79], v[116:119], 0
	v_min3_i32 v160, v120, v121, v156
	v_min3_i32 v160, v122, v123, v160
	v_min3_i32 v160, v124, v125, v160
	v_min3_i32 v160, v126, v127, v160
	v_min3_i32 v160, v128, v129, v160
	v_min3_i32 v160, v130, v131, v160
	v_min3_i32 v160, v132, v133, v160
	v_min3_i32 v157, v134, v135, v160
	v_cmp_ge_i32_e32 vcc, v157, v156
	v_mfma_f32_16x16x32_f16 v[120:123], v[80:83], v[116:119], 0
	v_mfma_f32_16x16x32_f16 v[124:127], v[84:87], v[116:119], 0
	v_cndmask_b32_e32 v158, 2, v158, vcc
	v_mfma_f32_16x16x32_f16 v[128:131], v[88:91], v[116:119], 0
	v_mfma_f32_16x16x32_f16 v[132:135], v[92:95], v[116:119], 0
	v_min3_i32 v160, v136, v137, v157
	v_min3_i32 v160, v138, v139, v160
	v_min3_i32 v160, v140, v141, v160
	v_min3_i32 v160, v142, v143, v160
	v_min3_i32 v160, v144, v145, v160
	v_min3_i32 v160, v146, v147, v160
	v_min3_i32 v160, v148, v149, v160
	v_min3_i32 v156, v150, v151, v160
	v_cmp_ge_i32_e32 vcc, v156, v157
	v_mfma_f32_16x16x32_f16 v[136:139], v[96:99], v[116:119], 0
	v_mfma_f32_16x16x32_f16 v[140:143], v[100:103], v[116:119], 0
	v_cndmask_b32_e32 v158, 3, v158, vcc
	v_mfma_f32_16x16x32_f16 v[144:147], v[104:107], v[116:119], 0
	v_mfma_f32_16x16x32_f16 v[148:151], v[108:111], v[116:119], 0
	v_min3_i32 v160, v120, v121, v156
	v_min3_i32 v160, v122, v123, v160
	v_min3_i32 v160, v124, v125, v160
	v_min3_i32 v160, v126, v127, v160
	v_min3_i32 v160, v128, v129, v160
	v_min3_i32 v160, v130, v131, v160
	v_min3_i32 v160, v132, v133, v160
	v_min3_i32 v157, v134, v135, v160
	v_cmp_ge_i32_e32 vcc, v157, v156
	s_waitcnt vmcnt(0)
	global_load_dwordx4 v[116:119], v164, s[4:5] offset:3072
	v_mfma_f32_16x16x32_f16 v[120:123], v[16:19], v[112:115], 0
	v_mfma_f32_16x16x32_f16 v[124:127], v[20:23], v[112:115], 0
	v_cndmask_b32_e32 v158, 4, v158, vcc
	v_mfma_f32_16x16x32_f16 v[128:131], v[24:27], v[112:115], 0
	v_mfma_f32_16x16x32_f16 v[132:135], v[28:31], v[112:115], 0
	v_min3_i32 v160, v136, v137, v157
	v_min3_i32 v160, v138, v139, v160
	v_min3_i32 v160, v140, v141, v160
	v_min3_i32 v160, v142, v143, v160
	v_min3_i32 v160, v144, v145, v160
	v_min3_i32 v160, v146, v147, v160
	v_min3_i32 v160, v148, v149, v160
	v_min3_i32 v156, v150, v151, v160
	v_cmp_ge_i32_e32 vcc, v156, v157
	v_mfma_f32_16x16x32_f16 v[136:139], v[32:35], v[112:115], 0
	v_mfma_f32_16x16x32_f16 v[140:143], v[36:39], v[112:115], 0
	v_cndmask_b32_e32 v158, 5, v158, vcc
	v_add_u32_e32 v162, s40, v158
	v_lshl_or_b32 v162, v162, 2, v166
	v_mov_b32_e32 v163, v156
	ds_min_u64 v167, v[162:163] offset:16512
	v_mfma_f32_16x16x32_f16 v[144:147], v[40:43], v[112:115], 0
	v_mfma_f32_16x16x32_f16 v[148:151], v[44:47], v[112:115], 0
	v_min3_i32 v160, v120, v121, s41
	v_min3_i32 v160, v122, v123, v160
	v_min3_i32 v160, v124, v125, v160
	v_min3_i32 v160, v126, v127, v160
	v_min3_i32 v160, v128, v129, v160
	v_min3_i32 v160, v130, v131, v160
	v_min3_i32 v160, v132, v133, v160
	v_min3_i32 v157, v134, v135, v160
	v_mfma_f32_16x16x32_f16 v[120:123], v[48:51], v[112:115], 0
	v_mfma_f32_16x16x32_f16 v[124:127], v[52:55], v[112:115], 0
	v_mov_b32_e32 v158, 0
	v_mfma_f32_16x16x32_f16 v[128:131], v[56:59], v[112:115], 0
	v_mfma_f32_16x16x32_f16 v[132:135], v[60:63], v[112:115], 0
	v_min3_i32 v160, v136, v137, v157
	v_min3_i32 v160, v138, v139, v160
	v_min3_i32 v160, v140, v141, v160
	v_min3_i32 v160, v142, v143, v160
	v_min3_i32 v160, v144, v145, v160
	v_min3_i32 v160, v146, v147, v160
	v_min3_i32 v160, v148, v149, v160
	v_min3_i32 v156, v150, v151, v160
	v_cmp_ge_i32_e32 vcc, v156, v157
	v_mfma_f32_16x16x32_f16 v[136:139], v[64:67], v[112:115], 0
	v_mfma_f32_16x16x32_f16 v[140:143], v[68:71], v[112:115], 0
	v_cndmask_b32_e32 v158, 1, v158, vcc
	v_mfma_f32_16x16x32_f16 v[144:147], v[72:75], v[112:115], 0
	v_mfma_f32_16x16x32_f16 v[148:151], v[76:79], v[112:115], 0
	v_min3_i32 v160, v120, v121, v156
	v_min3_i32 v160, v122, v123, v160
	v_min3_i32 v160, v124, v125, v160
	v_min3_i32 v160, v126, v127, v160
	v_min3_i32 v160, v128, v129, v160
	v_min3_i32 v160, v130, v131, v160
	v_min3_i32 v160, v132, v133, v160
	v_min3_i32 v157, v134, v135, v160
	v_cmp_ge_i32_e32 vcc, v157, v156
	v_mfma_f32_16x16x32_f16 v[120:123], v[80:83], v[112:115], 0
	v_mfma_f32_16x16x32_f16 v[124:127], v[84:87], v[112:115], 0
	v_cndmask_b32_e32 v158, 2, v158, vcc
	v_mfma_f32_16x16x32_f16 v[128:131], v[88:91], v[112:115], 0
	v_mfma_f32_16x16x32_f16 v[132:135], v[92:95], v[112:115], 0
	v_min3_i32 v160, v136, v137, v157
	v_min3_i32 v160, v138, v139, v160
	v_min3_i32 v160, v140, v141, v160
	v_min3_i32 v160, v142, v143, v160
	v_min3_i32 v160, v144, v145, v160
	v_min3_i32 v160, v146, v147, v160
	v_min3_i32 v160, v148, v149, v160
	v_min3_i32 v156, v150, v151, v160
	v_cmp_ge_i32_e32 vcc, v156, v157
	v_mfma_f32_16x16x32_f16 v[136:139], v[96:99], v[112:115], 0
	v_mfma_f32_16x16x32_f16 v[140:143], v[100:103], v[112:115], 0
	v_cndmask_b32_e32 v158, 3, v158, vcc
	v_mfma_f32_16x16x32_f16 v[144:147], v[104:107], v[112:115], 0
	v_mfma_f32_16x16x32_f16 v[148:151], v[108:111], v[112:115], 0
	v_min3_i32 v160, v120, v121, v156
	v_min3_i32 v160, v122, v123, v160
	v_min3_i32 v160, v124, v125, v160
	v_min3_i32 v160, v126, v127, v160
	v_min3_i32 v160, v128, v129, v160
	v_min3_i32 v160, v130, v131, v160
	v_min3_i32 v160, v132, v133, v160
	v_min3_i32 v157, v134, v135, v160
	v_cmp_ge_i32_e32 vcc, v157, v156
	s_waitcnt vmcnt(0)
	global_load_dwordx4 v[112:115], v164, s[22:23]
	v_mfma_f32_16x16x32_f16 v[120:123], v[16:19], v[116:119], 0
	v_mfma_f32_16x16x32_f16 v[124:127], v[20:23], v[116:119], 0
	v_cndmask_b32_e32 v158, 4, v158, vcc
	v_mfma_f32_16x16x32_f16 v[128:131], v[24:27], v[116:119], 0
	v_mfma_f32_16x16x32_f16 v[132:135], v[28:31], v[116:119], 0
	v_min3_i32 v160, v136, v137, v157
	v_min3_i32 v160, v138, v139, v160
	v_min3_i32 v160, v140, v141, v160
	v_min3_i32 v160, v142, v143, v160
	v_min3_i32 v160, v144, v145, v160
	v_min3_i32 v160, v146, v147, v160
	v_min3_i32 v160, v148, v149, v160
	v_min3_i32 v156, v150, v151, v160
	v_cmp_ge_i32_e32 vcc, v156, v157
	v_mfma_f32_16x16x32_f16 v[136:139], v[32:35], v[116:119], 0
	v_mfma_f32_16x16x32_f16 v[140:143], v[36:39], v[116:119], 0
	v_cndmask_b32_e32 v158, 5, v158, vcc
	v_add_u32_e32 v162, s40, v158
	v_lshl_or_b32 v162, v162, 2, v166
	v_mov_b32_e32 v163, v156
	ds_min_u64 v167, v[162:163] offset:16640
	v_mfma_f32_16x16x32_f16 v[144:147], v[40:43], v[116:119], 0
	v_mfma_f32_16x16x32_f16 v[148:151], v[44:47], v[116:119], 0
	v_min3_i32 v160, v120, v121, s41
	v_min3_i32 v160, v122, v123, v160
	v_min3_i32 v160, v124, v125, v160
	v_min3_i32 v160, v126, v127, v160
	v_min3_i32 v160, v128, v129, v160
	v_min3_i32 v160, v130, v131, v160
	v_min3_i32 v160, v132, v133, v160
	v_min3_i32 v157, v134, v135, v160
	v_mfma_f32_16x16x32_f16 v[120:123], v[48:51], v[116:119], 0
	v_mfma_f32_16x16x32_f16 v[124:127], v[52:55], v[116:119], 0
	v_mov_b32_e32 v158, 0
	v_mfma_f32_16x16x32_f16 v[128:131], v[56:59], v[116:119], 0
	v_mfma_f32_16x16x32_f16 v[132:135], v[60:63], v[116:119], 0
	v_min3_i32 v160, v136, v137, v157
	v_min3_i32 v160, v138, v139, v160
	v_min3_i32 v160, v140, v141, v160
	v_min3_i32 v160, v142, v143, v160
	v_min3_i32 v160, v144, v145, v160
	v_min3_i32 v160, v146, v147, v160
	v_min3_i32 v160, v148, v149, v160
	v_min3_i32 v156, v150, v151, v160
	v_cmp_ge_i32_e32 vcc, v156, v157
	v_mfma_f32_16x16x32_f16 v[136:139], v[64:67], v[116:119], 0
	v_mfma_f32_16x16x32_f16 v[140:143], v[68:71], v[116:119], 0
	v_cndmask_b32_e32 v158, 1, v158, vcc
	v_mfma_f32_16x16x32_f16 v[144:147], v[72:75], v[116:119], 0
	v_mfma_f32_16x16x32_f16 v[148:151], v[76:79], v[116:119], 0
	v_min3_i32 v160, v120, v121, v156
	v_min3_i32 v160, v122, v123, v160
	v_min3_i32 v160, v124, v125, v160
	v_min3_i32 v160, v126, v127, v160
	v_min3_i32 v160, v128, v129, v160
	v_min3_i32 v160, v130, v131, v160
	v_min3_i32 v160, v132, v133, v160
	v_min3_i32 v157, v134, v135, v160
	v_cmp_ge_i32_e32 vcc, v157, v156
	v_mfma_f32_16x16x32_f16 v[120:123], v[80:83], v[116:119], 0
	v_mfma_f32_16x16x32_f16 v[124:127], v[84:87], v[116:119], 0
	v_cndmask_b32_e32 v158, 2, v158, vcc
	v_mfma_f32_16x16x32_f16 v[128:131], v[88:91], v[116:119], 0
	v_mfma_f32_16x16x32_f16 v[132:135], v[92:95], v[116:119], 0
	v_min3_i32 v160, v136, v137, v157
	v_min3_i32 v160, v138, v139, v160
	v_min3_i32 v160, v140, v141, v160
	v_min3_i32 v160, v142, v143, v160
	v_min3_i32 v160, v144, v145, v160
	v_min3_i32 v160, v146, v147, v160
	v_min3_i32 v160, v148, v149, v160
	v_min3_i32 v156, v150, v151, v160
	v_cmp_ge_i32_e32 vcc, v156, v157
	v_mfma_f32_16x16x32_f16 v[136:139], v[96:99], v[116:119], 0
	v_mfma_f32_16x16x32_f16 v[140:143], v[100:103], v[116:119], 0
	v_cndmask_b32_e32 v158, 3, v158, vcc
	v_mfma_f32_16x16x32_f16 v[144:147], v[104:107], v[116:119], 0
	v_mfma_f32_16x16x32_f16 v[148:151], v[108:111], v[116:119], 0
	v_min3_i32 v160, v120, v121, v156
	v_min3_i32 v160, v122, v123, v160
	v_min3_i32 v160, v124, v125, v160
	v_min3_i32 v160, v126, v127, v160
	v_min3_i32 v160, v128, v129, v160
	v_min3_i32 v160, v130, v131, v160
	v_min3_i32 v160, v132, v133, v160
	v_min3_i32 v157, v134, v135, v160
	v_cmp_ge_i32_e32 vcc, v157, v156
	s_waitcnt vmcnt(0)
	global_load_dwordx4 v[116:119], v164, s[22:23] offset:1024
	v_mfma_f32_16x16x32_f16 v[120:123], v[16:19], v[112:115], 0
	v_mfma_f32_16x16x32_f16 v[124:127], v[20:23], v[112:115], 0
	v_cndmask_b32_e32 v158, 4, v158, vcc
	v_mfma_f32_16x16x32_f16 v[128:131], v[24:27], v[112:115], 0
	v_mfma_f32_16x16x32_f16 v[132:135], v[28:31], v[112:115], 0
	v_min3_i32 v160, v136, v137, v157
	v_min3_i32 v160, v138, v139, v160
	v_min3_i32 v160, v140, v141, v160
	v_min3_i32 v160, v142, v143, v160
	v_min3_i32 v160, v144, v145, v160
	v_min3_i32 v160, v146, v147, v160
	v_min3_i32 v160, v148, v149, v160
	v_min3_i32 v156, v150, v151, v160
	v_cmp_ge_i32_e32 vcc, v156, v157
	v_mfma_f32_16x16x32_f16 v[136:139], v[32:35], v[112:115], 0
	v_mfma_f32_16x16x32_f16 v[140:143], v[36:39], v[112:115], 0
	v_cndmask_b32_e32 v158, 5, v158, vcc
	v_add_u32_e32 v162, s40, v158
	v_lshl_or_b32 v162, v162, 2, v166
	v_mov_b32_e32 v163, v156
	ds_min_u64 v167, v[162:163] offset:16768
	v_mfma_f32_16x16x32_f16 v[144:147], v[40:43], v[112:115], 0
	v_mfma_f32_16x16x32_f16 v[148:151], v[44:47], v[112:115], 0
	v_min3_i32 v160, v120, v121, s41
	v_min3_i32 v160, v122, v123, v160
	v_min3_i32 v160, v124, v125, v160
	v_min3_i32 v160, v126, v127, v160
	v_min3_i32 v160, v128, v129, v160
	v_min3_i32 v160, v130, v131, v160
	v_min3_i32 v160, v132, v133, v160
	v_min3_i32 v157, v134, v135, v160
	v_mfma_f32_16x16x32_f16 v[120:123], v[48:51], v[112:115], 0
	v_mfma_f32_16x16x32_f16 v[124:127], v[52:55], v[112:115], 0
	v_mov_b32_e32 v158, 0
	v_mfma_f32_16x16x32_f16 v[128:131], v[56:59], v[112:115], 0
	v_mfma_f32_16x16x32_f16 v[132:135], v[60:63], v[112:115], 0
	v_min3_i32 v160, v136, v137, v157
	v_min3_i32 v160, v138, v139, v160
	v_min3_i32 v160, v140, v141, v160
	v_min3_i32 v160, v142, v143, v160
	v_min3_i32 v160, v144, v145, v160
	v_min3_i32 v160, v146, v147, v160
	v_min3_i32 v160, v148, v149, v160
	v_min3_i32 v156, v150, v151, v160
	v_cmp_ge_i32_e32 vcc, v156, v157
	v_mfma_f32_16x16x32_f16 v[136:139], v[64:67], v[112:115], 0
	v_mfma_f32_16x16x32_f16 v[140:143], v[68:71], v[112:115], 0
	v_cndmask_b32_e32 v158, 1, v158, vcc
	v_mfma_f32_16x16x32_f16 v[144:147], v[72:75], v[112:115], 0
	v_mfma_f32_16x16x32_f16 v[148:151], v[76:79], v[112:115], 0
	v_min3_i32 v160, v120, v121, v156
	v_min3_i32 v160, v122, v123, v160
	v_min3_i32 v160, v124, v125, v160
	v_min3_i32 v160, v126, v127, v160
	v_min3_i32 v160, v128, v129, v160
	v_min3_i32 v160, v130, v131, v160
	v_min3_i32 v160, v132, v133, v160
	v_min3_i32 v157, v134, v135, v160
	v_cmp_ge_i32_e32 vcc, v157, v156
	v_mfma_f32_16x16x32_f16 v[120:123], v[80:83], v[112:115], 0
	v_mfma_f32_16x16x32_f16 v[124:127], v[84:87], v[112:115], 0
	v_cndmask_b32_e32 v158, 2, v158, vcc
	v_mfma_f32_16x16x32_f16 v[128:131], v[88:91], v[112:115], 0
	v_mfma_f32_16x16x32_f16 v[132:135], v[92:95], v[112:115], 0
	v_min3_i32 v160, v136, v137, v157
	v_min3_i32 v160, v138, v139, v160
	v_min3_i32 v160, v140, v141, v160
	v_min3_i32 v160, v142, v143, v160
	v_min3_i32 v160, v144, v145, v160
	v_min3_i32 v160, v146, v147, v160
	v_min3_i32 v160, v148, v149, v160
	v_min3_i32 v156, v150, v151, v160
	v_cmp_ge_i32_e32 vcc, v156, v157
	v_mfma_f32_16x16x32_f16 v[136:139], v[96:99], v[112:115], 0
	v_mfma_f32_16x16x32_f16 v[140:143], v[100:103], v[112:115], 0
	v_cndmask_b32_e32 v158, 3, v158, vcc
	v_mfma_f32_16x16x32_f16 v[144:147], v[104:107], v[112:115], 0
	v_mfma_f32_16x16x32_f16 v[148:151], v[108:111], v[112:115], 0
	v_min3_i32 v160, v120, v121, v156
	v_min3_i32 v160, v122, v123, v160
	v_min3_i32 v160, v124, v125, v160
	v_min3_i32 v160, v126, v127, v160
	v_min3_i32 v160, v128, v129, v160
	v_min3_i32 v160, v130, v131, v160
	v_min3_i32 v160, v132, v133, v160
	v_min3_i32 v157, v134, v135, v160
	v_cmp_ge_i32_e32 vcc, v157, v156
	s_waitcnt vmcnt(0)
	global_load_dwordx4 v[112:115], v164, s[22:23] offset:2048
	v_mfma_f32_16x16x32_f16 v[120:123], v[16:19], v[116:119], 0
	v_mfma_f32_16x16x32_f16 v[124:127], v[20:23], v[116:119], 0
	v_cndmask_b32_e32 v158, 4, v158, vcc
	v_mfma_f32_16x16x32_f16 v[128:131], v[24:27], v[116:119], 0
	v_mfma_f32_16x16x32_f16 v[132:135], v[28:31], v[116:119], 0
	v_min3_i32 v160, v136, v137, v157
	v_min3_i32 v160, v138, v139, v160
	v_min3_i32 v160, v140, v141, v160
	v_min3_i32 v160, v142, v143, v160
	v_min3_i32 v160, v144, v145, v160
	v_min3_i32 v160, v146, v147, v160
	v_min3_i32 v160, v148, v149, v160
	v_min3_i32 v156, v150, v151, v160
	v_cmp_ge_i32_e32 vcc, v156, v157
	v_mfma_f32_16x16x32_f16 v[136:139], v[32:35], v[116:119], 0
	v_mfma_f32_16x16x32_f16 v[140:143], v[36:39], v[116:119], 0
	v_cndmask_b32_e32 v158, 5, v158, vcc
	v_add_u32_e32 v162, s40, v158
	v_lshl_or_b32 v162, v162, 2, v166
	v_mov_b32_e32 v163, v156
	ds_min_u64 v167, v[162:163] offset:16896
	v_mfma_f32_16x16x32_f16 v[144:147], v[40:43], v[116:119], 0
	v_mfma_f32_16x16x32_f16 v[148:151], v[44:47], v[116:119], 0
	v_min3_i32 v160, v120, v121, s41
	v_min3_i32 v160, v122, v123, v160
	v_min3_i32 v160, v124, v125, v160
	v_min3_i32 v160, v126, v127, v160
	v_min3_i32 v160, v128, v129, v160
	v_min3_i32 v160, v130, v131, v160
	v_min3_i32 v160, v132, v133, v160
	v_min3_i32 v157, v134, v135, v160
	v_mfma_f32_16x16x32_f16 v[120:123], v[48:51], v[116:119], 0
	v_mfma_f32_16x16x32_f16 v[124:127], v[52:55], v[116:119], 0
	v_mov_b32_e32 v158, 0
	v_mfma_f32_16x16x32_f16 v[128:131], v[56:59], v[116:119], 0
	v_mfma_f32_16x16x32_f16 v[132:135], v[60:63], v[116:119], 0
	v_min3_i32 v160, v136, v137, v157
	v_min3_i32 v160, v138, v139, v160
	v_min3_i32 v160, v140, v141, v160
	v_min3_i32 v160, v142, v143, v160
	v_min3_i32 v160, v144, v145, v160
	v_min3_i32 v160, v146, v147, v160
	v_min3_i32 v160, v148, v149, v160
	v_min3_i32 v156, v150, v151, v160
	v_cmp_ge_i32_e32 vcc, v156, v157
	v_mfma_f32_16x16x32_f16 v[136:139], v[64:67], v[116:119], 0
	v_mfma_f32_16x16x32_f16 v[140:143], v[68:71], v[116:119], 0
	v_cndmask_b32_e32 v158, 1, v158, vcc
	v_mfma_f32_16x16x32_f16 v[144:147], v[72:75], v[116:119], 0
	v_mfma_f32_16x16x32_f16 v[148:151], v[76:79], v[116:119], 0
	v_min3_i32 v160, v120, v121, v156
	v_min3_i32 v160, v122, v123, v160
	v_min3_i32 v160, v124, v125, v160
	v_min3_i32 v160, v126, v127, v160
	v_min3_i32 v160, v128, v129, v160
	v_min3_i32 v160, v130, v131, v160
	v_min3_i32 v160, v132, v133, v160
	v_min3_i32 v157, v134, v135, v160
	v_cmp_ge_i32_e32 vcc, v157, v156
	v_mfma_f32_16x16x32_f16 v[120:123], v[80:83], v[116:119], 0
	v_mfma_f32_16x16x32_f16 v[124:127], v[84:87], v[116:119], 0
	v_cndmask_b32_e32 v158, 2, v158, vcc
	v_mfma_f32_16x16x32_f16 v[128:131], v[88:91], v[116:119], 0
	v_mfma_f32_16x16x32_f16 v[132:135], v[92:95], v[116:119], 0
	v_min3_i32 v160, v136, v137, v157
	v_min3_i32 v160, v138, v139, v160
	v_min3_i32 v160, v140, v141, v160
	v_min3_i32 v160, v142, v143, v160
	v_min3_i32 v160, v144, v145, v160
	v_min3_i32 v160, v146, v147, v160
	v_min3_i32 v160, v148, v149, v160
	v_min3_i32 v156, v150, v151, v160
	v_cmp_ge_i32_e32 vcc, v156, v157
	v_mfma_f32_16x16x32_f16 v[136:139], v[96:99], v[116:119], 0
	v_mfma_f32_16x16x32_f16 v[140:143], v[100:103], v[116:119], 0
	v_cndmask_b32_e32 v158, 3, v158, vcc
	v_mfma_f32_16x16x32_f16 v[144:147], v[104:107], v[116:119], 0
	v_mfma_f32_16x16x32_f16 v[148:151], v[108:111], v[116:119], 0
	v_min3_i32 v160, v120, v121, v156
	v_min3_i32 v160, v122, v123, v160
	v_min3_i32 v160, v124, v125, v160
	v_min3_i32 v160, v126, v127, v160
	v_min3_i32 v160, v128, v129, v160
	v_min3_i32 v160, v130, v131, v160
	v_min3_i32 v160, v132, v133, v160
	v_min3_i32 v157, v134, v135, v160
	v_cmp_ge_i32_e32 vcc, v157, v156
	s_waitcnt vmcnt(0)
	global_load_dwordx4 v[116:119], v164, s[22:23] offset:3072
	v_mfma_f32_16x16x32_f16 v[120:123], v[16:19], v[112:115], 0
	v_mfma_f32_16x16x32_f16 v[124:127], v[20:23], v[112:115], 0
	v_cndmask_b32_e32 v158, 4, v158, vcc
	v_mfma_f32_16x16x32_f16 v[128:131], v[24:27], v[112:115], 0
	v_mfma_f32_16x16x32_f16 v[132:135], v[28:31], v[112:115], 0
	v_min3_i32 v160, v136, v137, v157
	v_min3_i32 v160, v138, v139, v160
	v_min3_i32 v160, v140, v141, v160
	v_min3_i32 v160, v142, v143, v160
	v_min3_i32 v160, v144, v145, v160
	v_min3_i32 v160, v146, v147, v160
	v_min3_i32 v160, v148, v149, v160
	v_min3_i32 v156, v150, v151, v160
	v_cmp_ge_i32_e32 vcc, v156, v157
	v_mfma_f32_16x16x32_f16 v[136:139], v[32:35], v[112:115], 0
	v_mfma_f32_16x16x32_f16 v[140:143], v[36:39], v[112:115], 0
	v_cndmask_b32_e32 v158, 5, v158, vcc
	v_add_u32_e32 v162, s40, v158
	v_lshl_or_b32 v162, v162, 2, v166
	v_mov_b32_e32 v163, v156
	ds_min_u64 v167, v[162:163] offset:17024
	v_mfma_f32_16x16x32_f16 v[144:147], v[40:43], v[112:115], 0
	v_mfma_f32_16x16x32_f16 v[148:151], v[44:47], v[112:115], 0
	v_min3_i32 v160, v120, v121, s41
	v_min3_i32 v160, v122, v123, v160
	v_min3_i32 v160, v124, v125, v160
	v_min3_i32 v160, v126, v127, v160
	v_min3_i32 v160, v128, v129, v160
	v_min3_i32 v160, v130, v131, v160
	v_min3_i32 v160, v132, v133, v160
	v_min3_i32 v157, v134, v135, v160
	s_waitcnt lgkmcnt(0)
	s_barrier
	s_lshl_b32 s60, s50, 7
	v_add_u32_e32 v2, s60, v169
	ds_read_b32 v178, v2 offset:16384
	s_lshl_b32 s60, s50, 10
	v_add_u32_e32 v210, s60, v170
	s_cmp_lt_u32 s50, 2
	s_cbranch_scc0 .Lp1a_y
	s_add_i32 s65, s50, 4
	s_lshl_b32 s60, s65, 7
	v_add_u32_e32 v2, s60, v169
	ds_read_b32 v216, v2 offset:16384
	s_lshl_b32 s60, s65, 10
	v_add_u32_e32 v248, s60, v170
